# K1 prologue de-serialised: src/dst loads issued before the LDS counter zeroing loop
# baseline (speedup 1.0000x reference)
.LBB0_6:
	s_mul_i32 s34, s2, 0x30d4
	v_lshrrev_b32_e32 v53, 6, v0
	s_movk_i32 s0, 0x30e
	v_mov_b32_e32 v1, s34
	v_mad_u32_u24 v3, v53, s0, v1
	v_and_b32_e32 v2, 63, v0
	s_add_i32 s0, s34, 0x30d4
	v_add_u32_e32 v4, 0x30e, v3
	v_min_i32_e32 v8, s0, v4
	v_add_u32_e32 v3, v3, v2
	v_cmp_lt_i32_e64 s[22:23], v3, v8
	v_mov_b32_e32 v60, 0
	v_mov_b32_e32 v78, 0
	v_cndmask_b32_e64 v4, v1, v3, s[22:23]
	v_ashrrev_i32_e32 v5, 31, v4
	v_lshlrev_b64 v[4:5], 2, v[4:5]
	s_waitcnt lgkmcnt(0)
	v_lshl_add_u64 v[6:7], s[28:29], 0, v[4:5]
	v_lshl_add_u64 v[4:5], s[30:31], 0, v[4:5]
	global_load_dword v52, v[4:5], off nt
	v_add_u32_e32 v4, 64, v3
	v_cmp_lt_i32_e64 s[20:21], v4, v8
	global_load_dword v51, v[6:7], off nt
	v_mov_b32_e32 v79, 0
	v_cndmask_b32_e64 v4, v1, v4, s[20:21]
	v_ashrrev_i32_e32 v5, 31, v4
	v_lshlrev_b64 v[4:5], 2, v[4:5]
	v_lshl_add_u64 v[6:7], s[28:29], 0, v[4:5]
	v_lshl_add_u64 v[4:5], s[30:31], 0, v[4:5]
	global_load_dword v50, v[4:5], off nt
	v_add_u32_e32 v4, 0x80, v3
	v_cmp_lt_i32_e64 s[18:19], v4, v8
	global_load_dword v49, v[6:7], off nt
	s_nop 0
	v_cndmask_b32_e64 v4, v1, v4, s[18:19]
	v_ashrrev_i32_e32 v5, 31, v4
	v_lshlrev_b64 v[4:5], 2, v[4:5]
	v_lshl_add_u64 v[6:7], s[28:29], 0, v[4:5]
	v_lshl_add_u64 v[4:5], s[30:31], 0, v[4:5]
	global_load_dword v48, v[4:5], off nt
	v_add_u32_e32 v4, 0xc0, v3
	v_cmp_lt_i32_e64 s[16:17], v4, v8
	global_load_dword v47, v[6:7], off nt
	s_nop 0
	v_cndmask_b32_e64 v4, v1, v4, s[16:17]
	v_ashrrev_i32_e32 v5, 31, v4
	v_lshlrev_b64 v[4:5], 2, v[4:5]
	v_lshl_add_u64 v[6:7], s[28:29], 0, v[4:5]
	v_lshl_add_u64 v[4:5], s[30:31], 0, v[4:5]
	global_load_dword v46, v[4:5], off nt
	v_add_u32_e32 v4, 0x100, v3
	v_cmp_lt_i32_e64 s[14:15], v4, v8
	global_load_dword v45, v[6:7], off nt
	s_nop 0
	v_cndmask_b32_e64 v4, v1, v4, s[14:15]
	v_ashrrev_i32_e32 v5, 31, v4
	v_lshlrev_b64 v[4:5], 2, v[4:5]
	v_lshl_add_u64 v[6:7], s[28:29], 0, v[4:5]
	v_lshl_add_u64 v[4:5], s[30:31], 0, v[4:5]
	global_load_dword v44, v[4:5], off nt
	v_add_u32_e32 v4, 0x140, v3
	v_cmp_lt_i32_e64 s[12:13], v4, v8
	global_load_dword v43, v[6:7], off nt
	s_nop 0
	v_cndmask_b32_e64 v4, v1, v4, s[12:13]
	v_ashrrev_i32_e32 v5, 31, v4
	v_lshlrev_b64 v[4:5], 2, v[4:5]
	v_lshl_add_u64 v[6:7], s[28:29], 0, v[4:5]
	v_lshl_add_u64 v[4:5], s[30:31], 0, v[4:5]
	global_load_dword v42, v[4:5], off nt
	v_add_u32_e32 v4, 0x180, v3
	v_cmp_lt_i32_e64 s[10:11], v4, v8
	global_load_dword v41, v[6:7], off nt
	s_nop 0
	v_cndmask_b32_e64 v4, v1, v4, s[10:11]
	v_ashrrev_i32_e32 v5, 31, v4
	v_lshlrev_b64 v[4:5], 2, v[4:5]
	v_lshl_add_u64 v[6:7], s[28:29], 0, v[4:5]
	v_lshl_add_u64 v[4:5], s[30:31], 0, v[4:5]
	global_load_dword v40, v[4:5], off nt
	v_add_u32_e32 v4, 0x1c0, v3
	v_cmp_lt_i32_e64 s[8:9], v4, v8
	global_load_dword v39, v[6:7], off nt
	s_nop 0
	v_cndmask_b32_e64 v4, v1, v4, s[8:9]
	v_ashrrev_i32_e32 v5, 31, v4
	v_lshlrev_b64 v[4:5], 2, v[4:5]
	v_lshl_add_u64 v[6:7], s[28:29], 0, v[4:5]
	v_lshl_add_u64 v[4:5], s[30:31], 0, v[4:5]
	global_load_dword v38, v[4:5], off nt
	v_add_u32_e32 v4, 0x200, v3
	v_cmp_lt_i32_e64 s[6:7], v4, v8
	global_load_dword v37, v[6:7], off nt
	s_nop 0
	v_cndmask_b32_e64 v4, v1, v4, s[6:7]
	v_ashrrev_i32_e32 v5, 31, v4
	v_lshlrev_b64 v[4:5], 2, v[4:5]
	v_lshl_add_u64 v[6:7], s[28:29], 0, v[4:5]
	v_lshl_add_u64 v[4:5], s[30:31], 0, v[4:5]
	global_load_dword v36, v[4:5], off nt
	v_add_u32_e32 v4, 0x240, v3
	v_cmp_lt_i32_e64 s[4:5], v4, v8
	global_load_dword v35, v[6:7], off nt
	s_nop 0
	v_cndmask_b32_e64 v4, v1, v4, s[4:5]
	v_ashrrev_i32_e32 v5, 31, v4
	v_lshlrev_b64 v[4:5], 2, v[4:5]
	v_lshl_add_u64 v[6:7], s[28:29], 0, v[4:5]
	v_lshl_add_u64 v[4:5], s[30:31], 0, v[4:5]
	global_load_dword v34, v[4:5], off nt
	v_add_u32_e32 v4, 0x280, v3
	v_cmp_lt_i32_e64 s[24:25], v4, v8
	global_load_dword v33, v[6:7], off nt
	s_nop 0
	v_cndmask_b32_e64 v4, v1, v4, s[24:25]
	v_ashrrev_i32_e32 v5, 31, v4
	v_lshlrev_b64 v[4:5], 2, v[4:5]
	v_lshl_add_u64 v[6:7], s[28:29], 0, v[4:5]
	v_lshl_add_u64 v[4:5], s[30:31], 0, v[4:5]
	global_load_dword v32, v[4:5], off nt
	v_add_u32_e32 v4, 0x2c0, v3
	v_cmp_lt_i32_e64 s[0:1], v4, v8
	v_add_u32_e32 v3, 0x300, v3
	global_load_dword v31, v[6:7], off nt
	v_cndmask_b32_e64 v4, v1, v4, s[0:1]
	v_ashrrev_i32_e32 v5, 31, v4
	v_lshlrev_b64 v[4:5], 2, v[4:5]
	v_lshl_add_u64 v[6:7], s[28:29], 0, v[4:5]
	v_lshl_add_u64 v[4:5], s[30:31], 0, v[4:5]
	v_cmp_lt_i32_e32 vcc, v3, v8
	global_load_dword v30, v[4:5], off nt
	global_load_dword v28, v[6:7], off nt
	v_cndmask_b32_e32 v4, v1, v3, vcc
	v_ashrrev_i32_e32 v5, 31, v4
	v_lshlrev_b64 v[4:5], 2, v[4:5]
	v_lshl_add_u64 v[6:7], s[28:29], 0, v[4:5]
	v_lshl_add_u64 v[4:5], s[30:31], 0, v[4:5]
	global_load_dword v1, v[6:7], off nt
	global_load_dword v26, v[4:5], off nt
	v_mov_b32_e32 v98, 0x12500
	v_or_b32_e32 v97, 0xfffffc00, v0
	v_lshl_add_u32 v98, v0, 2, v98
	s_mov_b64 s[46:47], 0
	v_mov_b32_e32 v99, 0
	s_movk_i32 s49, 0xbff
.Lk1_zero:
	v_add_u32_e32 v97, 0x400, v97
	v_cmp_lt_u32_e64 s[50:51], s49, v97
	ds_write2st64_b32 v98, v99, v99 offset1:64
	s_or_b64 s[46:47], s[50:51], s[46:47]
	v_add_u32_e32 v98, 0x1000, v98
	s_andn2_b64 exec, exec, s[46:47]
	s_cbranch_execnz .Lk1_zero
	s_or_b64 exec, exec, s[46:47]
	s_waitcnt lgkmcnt(0)
	v_lshlrev_b32_e32 v3, 10, v53
	v_add_u32_e32 v27, 0x12500, v3
	v_add_u32_e32 v29, 0x16500, v3
	s_barrier
	s_and_saveexec_b64 s[26:27], s[22:23]
	s_cbranch_execz .LBB0_10
	s_mov_b32 s3, 0x51eb851f
	s_waitcnt vmcnt(25)
	v_mul_hi_u32 v3, v52, s3
	v_lshrrev_b32_e32 v3, 5, v3
	v_and_b32_e32 v3, 0x3fffffc, v3
	v_add_u32_e32 v3, v27, v3
	v_mov_b32_e32 v4, 1
	ds_add_rtn_u32 v78, v3, v4
	s_waitcnt vmcnt(24)
	v_mul_hi_u32 v3, v51, s3
	v_lshrrev_b32_e32 v3, 5, v3
	v_and_b32_e32 v3, 0x3fffffc, v3
	v_add_u32_e32 v3, v29, v3
	ds_add_rtn_u32 v79, v3, v4
